# v36 + MoE2 K-loop: the eight next-tile weight loads issued as one burst at the end of the tile (counted waits 11..4) instead of one per MFMA group
# speedup vs baseline: 1.0192x; 1.0138x over previous
.Lrot_m2:
	ds_read_b64_tr_b16 v[210:211], v234
	ds_read_b64_tr_b16 v[212:213], v234 offset:2048
	ds_read_b64_tr_b16 v[214:215], v238
	ds_read_b64_tr_b16 v[216:217], v238 offset:2048
	ds_read_b128 v[162:165], v235
	ds_read_b128 v[166:169], v235 offset:2048
	ds_read_b64_tr_b16 v[218:219], v240
	ds_read_b64_tr_b16 v[220:221], v240 offset:2048
	ds_read_b64_tr_b16 v[222:223], v242
	ds_read_b64_tr_b16 v[224:225], v242 offset:2048
	s_waitcnt lgkmcnt(5)
	v_mfma_f32_16x16x32_bf16 v[34:37], v[210:213], v[162:165], v[34:37]
	ds_read_b128 v[226:229], v235 offset:4096
	s_and_b32 s42, s37, 0x8000
	v_add_u32_e32 v230, 0xffef8000, v209
	v_mfma_f32_16x16x32_bf16 v[38:41], v[214:217], v[162:165], v[38:41]
	s_add_i32 s43, s36, s39
	s_mov_b32 s44, m0
	s_mov_b32 m0, s43
	s_nop 0
	global_load_lds_dwordx4 v230, s[14:15]
	s_mov_b32 m0, s44
	s_waitcnt lgkmcnt(3)
	v_mfma_f32_16x16x32_bf16 v[42:45], v[218:221], v[162:165], v[42:45]
	s_waitcnt lgkmcnt(1)
	v_mfma_f32_16x16x32_bf16 v[46:49], v[222:225], v[162:165], v[46:49]
	v_mfma_f32_16x16x32_bf16 v[50:53], v[210:213], v[166:169], v[50:53]
	ds_read_b128 v[162:165], v235 offset:6144
	v_add_u32_e32 v230, 0xfff50000, v209
	s_add_i32 s44, s43, 0x2000
	v_mfma_f32_16x16x32_bf16 v[54:57], v[214:217], v[166:169], v[54:57]
	s_mov_b32 s45, m0
	s_mov_b32 m0, s44
	s_nop 0
	global_load_lds_dwordx4 v230, s[14:15]
	s_mov_b32 m0, s45
	v_mfma_f32_16x16x32_bf16 v[58:61], v[218:221], v[166:169], v[58:61]
	v_mfma_f32_16x16x32_bf16 v[62:65], v[222:225], v[166:169], v[62:65]
	s_waitcnt lgkmcnt(1)
	v_mfma_f32_16x16x32_bf16 v[66:69], v[210:213], v[226:229], v[66:69]
	ds_read_b128 v[166:169], v235 offset:8192
	v_add_u32_e32 v230, 0xfffa8000, v209
	s_add_i32 s44, s43, 0x4000
	v_mfma_f32_16x16x32_bf16 v[70:73], v[214:217], v[226:229], v[70:73]
	s_mov_b32 s45, m0
	s_mov_b32 m0, s44
	s_nop 0
	global_load_lds_dwordx4 v230, s[14:15]
	s_mov_b32 m0, s45
	v_mfma_f32_16x16x32_bf16 v[74:77], v[218:221], v[226:229], v[74:77]
	v_mfma_f32_16x16x32_bf16 v[78:81], v[222:225], v[226:229], v[78:81]
	s_waitcnt lgkmcnt(1)
	v_mfma_f32_16x16x32_bf16 v[82:85], v[210:213], v[162:165], v[82:85]
	ds_read_b128 v[226:229], v235 offset:10240
	s_addk_i32 s43, 0x6000
	s_mov_b32 s44, m0
	s_mov_b32 m0, s43
	s_nop 0
	global_load_lds_dwordx4 v209, s[14:15]
	s_mov_b32 m0, s44
	v_mfma_f32_16x16x32_bf16 v[86:89], v[214:217], v[162:165], v[86:89]
	v_mfma_f32_16x16x32_bf16 v[90:93], v[218:221], v[162:165], v[90:93]
	v_mfma_f32_16x16x32_bf16 v[94:97], v[222:225], v[162:165], v[94:97]
	ds_read_b128 v[230:233], v235 offset:12288
	ds_read_b64_tr_b16 v[162:163], v234 offset:16384
	ds_read_b64_tr_b16 v[164:165], v234 offset:18432
	s_waitcnt lgkmcnt(4)
	v_mfma_f32_16x16x32_bf16 v[98:101], v[210:213], v[166:169], v[98:101]
	v_mfma_f32_16x16x32_bf16 v[102:105], v[214:217], v[166:169], v[102:105]
	v_mfma_f32_16x16x32_bf16 v[106:109], v[218:221], v[166:169], v[106:109]
	v_mfma_f32_16x16x32_bf16 v[110:113], v[222:225], v[166:169], v[110:113]
	ds_read_b128 v[234:237], v235 offset:14336
	ds_read_b64_tr_b16 v[166:167], v238 offset:16384
	ds_read_b64_tr_b16 v[168:169], v238 offset:18432
	s_waitcnt lgkmcnt(6)
	v_mfma_f32_16x16x32_bf16 v[114:117], v[210:213], v[226:229], v[114:117]
	v_mfma_f32_16x16x32_bf16 v[118:121], v[214:217], v[226:229], v[118:121]
	v_mfma_f32_16x16x32_bf16 v[122:125], v[218:221], v[226:229], v[122:125]
	v_mfma_f32_16x16x32_bf16 v[126:129], v[222:225], v[226:229], v[126:129]
	v_add_u32_e32 v243, s41, v208
	ds_read_b128 v[226:229], v243
	ds_read_b64_tr_b16 v[238:239], v240 offset:16384
	ds_read_b64_tr_b16 v[240:241], v240 offset:18432
	s_waitcnt lgkmcnt(8)
	v_mfma_f32_16x16x32_bf16 v[130:133], v[210:213], v[230:233], v[130:133]
	v_mfma_f32_16x16x32_bf16 v[134:137], v[214:217], v[230:233], v[134:137]
	v_mfma_f32_16x16x32_bf16 v[138:141], v[218:221], v[230:233], v[138:141]
	v_mfma_f32_16x16x32_bf16 v[142:145], v[222:225], v[230:233], v[142:145]
	s_waitcnt lgkmcnt(5)
	v_mfma_f32_16x16x32_bf16 v[146:149], v[210:213], v[234:237], v[146:149]
	ds_read_b128 v[210:213], v243 offset:2048
	s_add_i32 s41, s24, s42
	v_mfma_f32_16x16x32_bf16 v[150:153], v[214:217], v[234:237], v[150:153]
	ds_read_b64_tr_b16 v[214:215], v242 offset:16384
	ds_read_b64_tr_b16 v[216:217], v242 offset:18432
	v_mfma_f32_16x16x32_bf16 v[158:161], v[218:221], v[234:237], v[158:161]
	v_mfma_f32_16x16x32_bf16 v[154:157], v[222:225], v[234:237], v[154:157]
	ds_read_b128 v[218:221], v243 offset:4096
	s_waitcnt lgkmcnt(6)
	v_mfma_f32_16x16x32_bf16 v[34:37], v[162:165], v[226:229], v[34:37]
	s_add_u32 s44, s2, s16
	s_waitcnt vmcnt(11)
	s_addc_u32 s45, s38, s17
	v_mfma_f32_16x16x32_bf16 v[38:41], v[166:169], v[226:229], v[38:41]
	v_cvt_pk_bf16_f32 v30, v30, v31
	v_cvt_pk_bf16_f32 v31, v32, v33
	v_add_u32_e32 v230, s41, v206
	s_waitcnt lgkmcnt(4)
	v_mfma_f32_16x16x32_bf16 v[42:45], v[238:241], v[226:229], v[42:45]
	ds_write_b64 v230, v[30:31]
	s_waitcnt lgkmcnt(2)
	v_mfma_f32_16x16x32_bf16 v[46:49], v[214:217], v[226:229], v[46:49]
	v_mfma_f32_16x16x32_bf16 v[50:53], v[162:165], v[210:213], v[50:53]
	ds_read_b128 v[222:225], v243 offset:6144
	s_waitcnt vmcnt(10)
	v_add_u32_e32 v226, s41, v205
	v_mfma_f32_16x16x32_bf16 v[54:57], v[166:169], v[210:213], v[54:57]
	v_cvt_pk_bf16_f32 v26, v26, v27
	v_cvt_pk_bf16_f32 v27, v28, v29
	v_mfma_f32_16x16x32_bf16 v[58:61], v[238:241], v[210:213], v[58:61]
	ds_write_b64 v226, v[26:27] offset:4096
	v_mfma_f32_16x16x32_bf16 v[62:65], v[214:217], v[210:213], v[62:65]
	s_waitcnt lgkmcnt(3)
	v_mfma_f32_16x16x32_bf16 v[66:69], v[162:165], v[218:221], v[66:69]
	ds_read_b128 v[210:213], v243 offset:8192
	s_waitcnt vmcnt(9)
	v_mfma_f32_16x16x32_bf16 v[70:73], v[166:169], v[218:221], v[70:73]
	v_cvt_pk_bf16_f32 v22, v22, v23
	v_cvt_pk_bf16_f32 v23, v24, v25
	ds_write_b64 v230, v[22:23] offset:8192
	v_mfma_f32_16x16x32_bf16 v[74:77], v[238:241], v[218:221], v[74:77]
	v_mfma_f32_16x16x32_bf16 v[78:81], v[214:217], v[218:221], v[78:81]
	s_waitcnt lgkmcnt(3)
	v_mfma_f32_16x16x32_bf16 v[82:85], v[162:165], v[222:225], v[82:85]
	ds_read_b128 v[218:221], v243 offset:10240
	s_waitcnt vmcnt(8)
	v_mfma_f32_16x16x32_bf16 v[86:89], v[166:169], v[222:225], v[86:89]
	v_cvt_pk_bf16_f32 v18, v18, v19
	v_cvt_pk_bf16_f32 v19, v20, v21
	ds_write_b64 v226, v[18:19] offset:12288
	v_mfma_f32_16x16x32_bf16 v[90:93], v[238:241], v[222:225], v[90:93]
	v_mfma_f32_16x16x32_bf16 v[94:97], v[214:217], v[222:225], v[94:97]
	s_waitcnt lgkmcnt(3)
	v_mfma_f32_16x16x32_bf16 v[98:101], v[162:165], v[210:213], v[98:101]
	ds_read_b128 v[222:225], v243 offset:12288
	s_waitcnt vmcnt(7)
	v_mfma_f32_16x16x32_bf16 v[102:105], v[166:169], v[210:213], v[102:105]
	v_cvt_pk_bf16_f32 v14, v14, v15
	v_cvt_pk_bf16_f32 v15, v16, v17
	ds_write_b64 v230, v[14:15] offset:16384
	v_mfma_f32_16x16x32_bf16 v[106:109], v[238:241], v[210:213], v[106:109]
	v_mfma_f32_16x16x32_bf16 v[110:113], v[214:217], v[210:213], v[110:113]
	s_waitcnt lgkmcnt(3)
	v_mfma_f32_16x16x32_bf16 v[114:117], v[162:165], v[218:221], v[114:117]
	ds_read_b128 v[210:213], v243 offset:14336
	s_waitcnt vmcnt(6)
	v_mfma_f32_16x16x32_bf16 v[118:121], v[166:169], v[218:221], v[118:121]
	v_cvt_pk_bf16_f32 v10, v10, v11
	v_cvt_pk_bf16_f32 v11, v12, v13
	ds_write_b64 v226, v[10:11] offset:20480
	v_mfma_f32_16x16x32_bf16 v[122:125], v[238:241], v[218:221], v[122:125]
	v_mfma_f32_16x16x32_bf16 v[126:129], v[214:217], v[218:221], v[126:129]
	s_waitcnt lgkmcnt(3)
	v_mfma_f32_16x16x32_bf16 v[130:133], v[162:165], v[222:225], v[130:133]
	s_waitcnt vmcnt(5)
	v_cvt_pk_bf16_f32 v6, v6, v7
	v_mfma_f32_16x16x32_bf16 v[134:137], v[166:169], v[222:225], v[134:137]
	v_cvt_pk_bf16_f32 v7, v8, v9
	ds_write_b64 v230, v[6:7] offset:24576
	v_mfma_f32_16x16x32_bf16 v[138:141], v[238:241], v[222:225], v[138:141]
	v_mfma_f32_16x16x32_bf16 v[142:145], v[214:217], v[222:225], v[142:145]
	s_waitcnt lgkmcnt(2)
	v_mfma_f32_16x16x32_bf16 v[146:149], v[162:165], v[210:213], v[146:149]
	s_waitcnt vmcnt(4)
	v_cvt_pk_bf16_f32 v2, v2, v3
	v_mfma_f32_16x16x32_bf16 v[150:153], v[166:169], v[210:213], v[150:153]
	v_cvt_pk_bf16_f32 v3, v4, v5
	ds_write_b64 v226, v[2:3] offset:28672
	v_mfma_f32_16x16x32_bf16 v[158:161], v[238:241], v[210:213], v[158:161]
	s_add_u32 s42, s44, 0x100000
	s_addc_u32 s43, s45, 0
	global_load_dwordx4 v[30:33], v199, s[42:43] nt
	s_add_u32 s42, s44, 0x110000
	s_addc_u32 s43, s45, 0
	global_load_dwordx4 v[26:29], v199, s[42:43] nt
	s_add_u32 s42, s44, 0x120000
	s_addc_u32 s43, s45, 0
	global_load_dwordx4 v[22:25], v199, s[42:43] nt
	s_add_u32 s42, s44, 0x130000
	s_addc_u32 s43, s45, 0
	global_load_dwordx4 v[18:21], v199, s[42:43] nt
	s_add_u32 s42, s44, 0x140000
	s_addc_u32 s43, s45, 0
	global_load_dwordx4 v[14:17], v199, s[42:43] nt
	s_add_u32 s42, s44, 0x150000
	s_addc_u32 s43, s45, 0
	global_load_dwordx4 v[10:13], v199, s[42:43] nt
	s_add_u32 s42, s44, 0x160000
	s_addc_u32 s43, s45, 0
	global_load_dwordx4 v[6:9], v199, s[42:43] nt
	s_add_u32 s42, s44, 0x170000
	s_addc_u32 s43, s45, 0
	global_load_dwordx4 v[2:5], v199, s[42:43] nt
	v_mfma_f32_16x16x32_bf16 v[154:157], v[214:217], v[210:213], v[154:157]
	s_add_i32 s41, s40, 0x8000
	s_cmp_lg_u32 s40, 0x10000
	s_cselect_b32 s40, s41, 0
	s_add_i32 s41, s39, 0x8000
	s_cmp_lg_u32 s39, 0x10000
	s_cselect_b32 s39, s41, 0
	s_add_u32 s16, s16, 0x80000
	s_addc_u32 s17, s17, 0
	s_add_i32 s37, s37, 0x8000
	v_add_u32_e32 v209, 0x80, v209
	s_add_i32 s42, s37, 0xffff8000
	s_and_b32 s42, s42, 0x8000
	s_add_i32 s41, s40, 0
	s_add_i32 s42, s24, s42
	v_add_u32_e32 v234, s42, v183
	v_add_u32_e32 v235, s41, v207
	v_add_u32_e32 v240, s42, v179
	v_add_u32_e32 v242, s42, v172
	v_add_u32_e32 v238, s42, v181
	s_waitcnt lgkmcnt(0)
	s_barrier
	s_cmp_lg_u32 s16, 0x1500000
	s_cbranch_scc1 .Lrot_m2
	v_add_u32_e32 v209, s24, v183
	v_add_u32_e32 v242, 0, v207
	v_add_u32_e32 v207, s24, v179
	v_add_u32_e32 v243, s24, v172
	v_add_u32_e32 v236, s24, v181
	ds_read_b64_tr_b16 v[162:163], v209
	ds_read_b64_tr_b16 v[164:165], v209 offset:2048
	ds_read_b64_tr_b16 v[166:167], v236
	ds_read_b64_tr_b16 v[168:169], v236 offset:2048
	ds_read_b128 v[210:213], v242
	ds_read_b128 v[214:217], v242 offset:2048
	ds_read_b64_tr_b16 v[218:219], v207
	ds_read_b64_tr_b16 v[220:221], v207 offset:2048
	ds_read_b64_tr_b16 v[222:223], v243
	ds_read_b64_tr_b16 v[224:225], v243 offset:2048
	s_waitcnt lgkmcnt(5)
	v_mfma_f32_16x16x32_bf16 v[34:37], v[162:165], v[210:213], v[34:37]
	ds_read_b128 v[226:229], v242 offset:4096
	v_mfma_f32_16x16x32_bf16 v[38:41], v[166:169], v[210:213], v[38:41]
	s_waitcnt lgkmcnt(3)
	v_mfma_f32_16x16x32_bf16 v[42:45], v[218:221], v[210:213], v[42:45]
	s_waitcnt lgkmcnt(1)
	v_mfma_f32_16x16x32_bf16 v[46:49], v[222:225], v[210:213], v[46:49]
	v_mfma_f32_16x16x32_bf16 v[50:53], v[162:165], v[214:217], v[50:53]
	ds_read_b128 v[210:213], v242 offset:6144
	v_mfma_f32_16x16x32_bf16 v[54:57], v[166:169], v[214:217], v[54:57]
	v_mfma_f32_16x16x32_bf16 v[58:61], v[218:221], v[214:217], v[58:61]
	v_mfma_f32_16x16x32_bf16 v[62:65], v[222:225], v[214:217], v[62:65]
	s_waitcnt lgkmcnt(1)
	v_mfma_f32_16x16x32_bf16 v[66:69], v[162:165], v[226:229], v[66:69]
	ds_read_b128 v[214:217], v242 offset:8192
	v_mfma_f32_16x16x32_bf16 v[70:73], v[166:169], v[226:229], v[70:73]
	v_mfma_f32_16x16x32_bf16 v[74:77], v[218:221], v[226:229], v[74:77]
	v_mfma_f32_16x16x32_bf16 v[78:81], v[222:225], v[226:229], v[78:81]
	s_waitcnt lgkmcnt(1)
	v_mfma_f32_16x16x32_bf16 v[82:85], v[162:165], v[210:213], v[82:85]
	ds_read_b128 v[226:229], v242 offset:10240
	v_mfma_f32_16x16x32_bf16 v[86:89], v[166:169], v[210:213], v[86:89]
	v_mfma_f32_16x16x32_bf16 v[90:93], v[218:221], v[210:213], v[90:93]
	v_mfma_f32_16x16x32_bf16 v[94:97], v[222:225], v[210:213], v[94:97]
	ds_read_b128 v[210:213], v242 offset:12288
	ds_read_b64_tr_b16 v[230:231], v209 offset:16384
	ds_read_b64_tr_b16 v[232:233], v209 offset:18432
	s_waitcnt lgkmcnt(4)
	v_mfma_f32_16x16x32_bf16 v[98:101], v[162:165], v[214:217], v[98:101]
	v_mfma_f32_16x16x32_bf16 v[102:105], v[166:169], v[214:217], v[102:105]
	v_mfma_f32_16x16x32_bf16 v[106:109], v[218:221], v[214:217], v[106:109]
	v_mfma_f32_16x16x32_bf16 v[110:113], v[222:225], v[214:217], v[110:113]
	ds_read_b128 v[214:217], v242 offset:14336
	ds_read_b64_tr_b16 v[234:235], v236 offset:16384
	ds_read_b64_tr_b16 v[236:237], v236 offset:18432
	s_waitcnt lgkmcnt(6)
	v_mfma_f32_16x16x32_bf16 v[114:117], v[162:165], v[226:229], v[114:117]
	v_mfma_f32_16x16x32_bf16 v[118:121], v[166:169], v[226:229], v[118:121]
	v_mfma_f32_16x16x32_bf16 v[122:125], v[218:221], v[226:229], v[122:125]
	v_mfma_f32_16x16x32_bf16 v[126:129], v[222:225], v[226:229], v[126:129]
	v_add_u32_e32 v244, 0, v208
	ds_read_b128 v[226:229], v244
	ds_read_b64_tr_b16 v[238:239], v207 offset:16384
	ds_read_b64_tr_b16 v[240:241], v207 offset:18432
	s_waitcnt lgkmcnt(8)
	v_mfma_f32_16x16x32_bf16 v[130:133], v[162:165], v[210:213], v[130:133]
	v_mfma_f32_16x16x32_bf16 v[134:137], v[166:169], v[210:213], v[134:137]
	v_mfma_f32_16x16x32_bf16 v[138:141], v[218:221], v[210:213], v[138:141]
	v_mfma_f32_16x16x32_bf16 v[142:145], v[222:225], v[210:213], v[142:145]
	s_waitcnt lgkmcnt(5)
	v_mfma_f32_16x16x32_bf16 v[146:149], v[162:165], v[214:217], v[146:149]
	v_mfma_f32_16x16x32_bf16 v[150:153], v[166:169], v[214:217], v[150:153]
	ds_read_b128 v[162:165], v244 offset:2048
	ds_read_b64_tr_b16 v[166:167], v243 offset:16384
	ds_read_b64_tr_b16 v[168:169], v243 offset:18432
	v_mfma_f32_16x16x32_bf16 v[158:161], v[218:221], v[214:217], v[158:161]
	v_mfma_f32_16x16x32_bf16 v[154:157], v[222:225], v[214:217], v[154:157]
	ds_read_b128 v[208:211], v244 offset:4096
	s_waitcnt vmcnt(7)
	v_add_u32_e32 v206, s25, v206
	v_cvt_pk_bf16_f32 v30, v30, v31
	v_cvt_pk_bf16_f32 v31, v32, v33
	s_waitcnt lgkmcnt(6)
	v_mfma_f32_16x16x32_bf16 v[34:37], v[230:233], v[226:229], v[34:37]
	ds_write_b64 v206, v[30:31]
	v_mfma_f32_16x16x32_bf16 v[38:41], v[234:237], v[226:229], v[38:41]
	s_waitcnt lgkmcnt(5)
	v_mfma_f32_16x16x32_bf16 v[42:45], v[238:241], v[226:229], v[42:45]
	s_waitcnt lgkmcnt(2)
	v_mfma_f32_16x16x32_bf16 v[30:33], v[166:169], v[226:229], v[46:49]
	v_mfma_f32_16x16x32_bf16 v[46:49], v[230:233], v[162:165], v[50:53]
	v_add_u32_e32 v205, s25, v205
	v_mfma_f32_16x16x32_bf16 v[50:53], v[234:237], v[162:165], v[54:57]
	s_nop 2
	ds_read_b128 v[54:57], v244 offset:6144
	s_waitcnt vmcnt(6)
	v_mfma_f32_16x16x32_bf16 v[58:61], v[238:241], v[162:165], v[58:61]
	v_cvt_pk_bf16_f32 v26, v26, v27
	v_cvt_pk_bf16_f32 v27, v28, v29
	ds_write_b64 v205, v[26:27] offset:4096
	v_mfma_f32_16x16x32_bf16 v[26:29], v[166:169], v[162:165], v[62:65]
	s_waitcnt lgkmcnt(3)
	v_mfma_f32_16x16x32_bf16 v[62:65], v[230:233], v[208:211], v[66:69]
	v_mfma_f32_16x16x32_bf16 v[66:69], v[234:237], v[208:211], v[70:73]
	s_nop 2
	ds_read_b128 v[70:73], v244 offset:8192
	s_waitcnt vmcnt(5)
	v_mfma_f32_16x16x32_bf16 v[74:77], v[238:241], v[208:211], v[74:77]
	v_cvt_pk_bf16_f32 v22, v22, v23
	v_cvt_pk_bf16_f32 v23, v24, v25
	ds_write_b64 v206, v[22:23] offset:8192
	v_mfma_f32_16x16x32_bf16 v[22:25], v[166:169], v[208:211], v[78:81]
	s_waitcnt lgkmcnt(3)
	v_mfma_f32_16x16x32_bf16 v[78:81], v[230:233], v[54:57], v[82:85]
	v_mfma_f32_16x16x32_bf16 v[82:85], v[234:237], v[54:57], v[86:89]
	s_nop 2
	ds_read_b128 v[86:89], v244 offset:10240
	s_waitcnt vmcnt(4)
	v_mfma_f32_16x16x32_bf16 v[90:93], v[238:241], v[54:57], v[90:93]
	v_cvt_pk_bf16_f32 v18, v18, v19
	v_cvt_pk_bf16_f32 v19, v20, v21
	ds_write_b64 v205, v[18:19] offset:12288
	v_mfma_f32_16x16x32_bf16 v[18:21], v[166:169], v[54:57], v[94:97]
	s_waitcnt lgkmcnt(3)
	v_mfma_f32_16x16x32_bf16 v[54:57], v[230:233], v[70:73], v[98:101]
	s_nop 2
	ds_read_b128 v[98:101], v244 offset:12288
	s_waitcnt vmcnt(3)
	v_mfma_f32_16x16x32_bf16 v[94:97], v[234:237], v[70:73], v[102:105]
	v_cvt_pk_bf16_f32 v14, v14, v15
	v_cvt_pk_bf16_f32 v15, v16, v17
	ds_write_b64 v206, v[14:15] offset:16384
	v_mfma_f32_16x16x32_bf16 v[102:105], v[238:241], v[70:73], v[106:109]
	v_mfma_f32_16x16x32_bf16 v[14:17], v[166:169], v[70:73], v[110:113]
	s_nop 2
	ds_read_b128 v[110:113], v244 offset:14336
	s_waitcnt vmcnt(2)
	s_waitcnt lgkmcnt(4)
	v_mfma_f32_16x16x32_bf16 v[70:73], v[230:233], v[86:89], v[114:117]
	v_cvt_pk_bf16_f32 v10, v10, v11
	v_cvt_pk_bf16_f32 v11, v12, v13
	ds_write_b64 v205, v[10:11] offset:20480
	v_mfma_f32_16x16x32_bf16 v[106:109], v[234:237], v[86:89], v[118:121]
	v_mfma_f32_16x16x32_bf16 v[114:117], v[238:241], v[86:89], v[122:125]
	v_mfma_f32_16x16x32_bf16 v[10:13], v[166:169], v[86:89], v[126:129]
	s_waitcnt vmcnt(1)
	s_waitcnt lgkmcnt(3)
	v_mfma_f32_16x16x32_bf16 v[86:89], v[230:233], v[98:101], v[130:133]
	v_cvt_pk_bf16_f32 v6, v6, v7
	v_cvt_pk_bf16_f32 v7, v8, v9
	ds_write_b64 v206, v[6:7] offset:24576
	v_mfma_f32_16x16x32_bf16 v[118:121], v[234:237], v[98:101], v[134:137]
	v_mfma_f32_16x16x32_bf16 v[122:125], v[238:241], v[98:101], v[138:141]
	v_mfma_f32_16x16x32_bf16 v[6:9], v[166:169], v[98:101], v[142:145]
	s_waitcnt vmcnt(0)
	s_waitcnt lgkmcnt(2)
	v_mfma_f32_16x16x32_bf16 v[98:101], v[230:233], v[110:113], v[146:149]
	v_cvt_pk_bf16_f32 v2, v2, v3
	v_cvt_pk_bf16_f32 v3, v4, v5
	ds_write_b64 v205, v[2:3] offset:28672
	v_mfma_f32_16x16x32_bf16 v[126:129], v[234:237], v[110:113], v[150:153]
	v_mfma_f32_16x16x32_bf16 v[130:133], v[238:241], v[110:113], v[158:161]
	v_mfma_f32_16x16x32_bf16 v[2:5], v[166:169], v[110:113], v[154:157]
	s_waitcnt lgkmcnt(0)
	s_barrier
	v_add_u32_e32 v168, s25, v183
	v_add_u32_e32 v181, s25, v181
	v_add_u32_e32 v179, s25, v179
	ds_read_b64_tr_b16 v[110:111], v168
	ds_read_b64_tr_b16 v[112:113], v168 offset:2048
	ds_read_b64_tr_b16 v[134:135], v181
	ds_read_b64_tr_b16 v[136:137], v181 offset:2048
	ds_read_b128 v[138:141], v242 offset:32768
	ds_read_b64_tr_b16 v[142:143], v179
	ds_read_b128 v[146:149], v242 offset:34816
	ds_read_b128 v[150:153], v242 offset:36864
	ds_read_b64_tr_b16 v[144:145], v179 offset:2048
	v_add_u32_e32 v172, s25, v172
	ds_read_b64_tr_b16 v[154:155], v172
	ds_read_b64_tr_b16 v[156:157], v172 offset:2048
	s_waitcnt lgkmcnt(6)
	v_mfma_f32_16x16x32_bf16 v[34:37], v[110:113], v[138:141], v[34:37]
	v_mfma_f32_16x16x32_bf16 v[38:41], v[134:137], v[138:141], v[38:41]
	s_waitcnt lgkmcnt(2)
	v_mfma_f32_16x16x32_bf16 v[42:45], v[142:145], v[138:141], v[42:45]
	s_waitcnt lgkmcnt(0)
	v_mfma_f32_16x16x32_bf16 v[30:33], v[154:157], v[138:141], v[30:33]
	v_mfma_f32_16x16x32_bf16 v[46:49], v[110:113], v[146:149], v[46:49]
	ds_read_b128 v[138:141], v242 offset:38912
	v_mfma_f32_16x16x32_bf16 v[50:53], v[134:137], v[146:149], v[50:53]
	v_mfma_f32_16x16x32_bf16 v[58:61], v[142:145], v[146:149], v[58:61]
	v_mfma_f32_16x16x32_bf16 v[26:29], v[154:157], v[146:149], v[26:29]
	v_mfma_f32_16x16x32_bf16 v[62:65], v[110:113], v[150:153], v[62:65]
	ds_read_b128 v[146:149], v242 offset:40960
	v_mfma_f32_16x16x32_bf16 v[66:69], v[134:137], v[150:153], v[66:69]
	v_mfma_f32_16x16x32_bf16 v[74:77], v[142:145], v[150:153], v[74:77]
	v_mfma_f32_16x16x32_bf16 v[22:25], v[154:157], v[150:153], v[22:25]
	s_waitcnt lgkmcnt(1)
	v_mfma_f32_16x16x32_bf16 v[150:153], v[134:137], v[138:141], v[82:85]
	s_nop 2
	ds_read_b128 v[82:85], v242 offset:43008
	v_mfma_f32_16x16x32_bf16 v[78:81], v[110:113], v[138:141], v[78:81]
	v_mfma_f32_16x16x32_bf16 v[18:21], v[154:157], v[138:141], v[18:21]
	v_mfma_f32_16x16x32_bf16 v[158:161], v[142:145], v[138:141], v[90:93]
	s_nop 2
	ds_read_b128 v[90:93], v242 offset:45056
	ds_read_b64_tr_b16 v[166:167], v168 offset:16384
	ds_read_b64_tr_b16 v[168:169], v168 offset:18432
	s_waitcnt lgkmcnt(4)
	v_mfma_f32_16x16x32_bf16 v[54:57], v[110:113], v[146:149], v[54:57]
	v_mfma_f32_16x16x32_bf16 v[14:17], v[154:157], v[146:149], v[14:17]
	v_mfma_f32_16x16x32_bf16 v[138:141], v[134:137], v[146:149], v[94:97]
	v_mfma_f32_16x16x32_bf16 v[162:165], v[142:145], v[146:149], v[102:105]
	s_waitcnt lgkmcnt(3)
	v_mfma_f32_16x16x32_bf16 v[146:149], v[110:113], v[82:85], v[70:73]
	s_nop 2
	ds_read_b128 v[70:73], v242 offset:47104
	ds_read_b64_tr_b16 v[214:215], v181 offset:16384
	ds_read_b64_tr_b16 v[216:217], v181 offset:18432
	v_mfma_f32_16x16x32_bf16 v[10:13], v[154:157], v[82:85], v[10:13]
	v_mfma_f32_16x16x32_bf16 v[206:209], v[134:137], v[82:85], v[106:109]
	v_mfma_f32_16x16x32_bf16 v[210:213], v[142:145], v[82:85], v[114:117]
	ds_read_b128 v[82:85], v244 offset:32768
	ds_read_b64_tr_b16 v[230:231], v179 offset:16384
	ds_read_b64_tr_b16 v[232:233], v179 offset:18432
	s_waitcnt lgkmcnt(8)
	v_mfma_f32_16x16x32_bf16 v[6:9], v[154:157], v[90:93], v[6:9]
	v_mfma_f32_16x16x32_bf16 v[218:221], v[110:113], v[90:93], v[86:89]
	v_mfma_f32_16x16x32_bf16 v[222:225], v[134:137], v[90:93], v[118:121]
	v_mfma_f32_16x16x32_bf16 v[226:229], v[142:145], v[90:93], v[122:125]
	s_waitcnt lgkmcnt(5)
	v_mfma_f32_16x16x32_bf16 v[130:133], v[142:145], v[70:73], v[130:133]
	ds_read_b128 v[86:89], v244 offset:34816
	ds_read_b64_tr_b16 v[142:143], v172 offset:16384
	ds_read_b64_tr_b16 v[144:145], v172 offset:18432
	v_mfma_f32_16x16x32_bf16 v[134:137], v[134:137], v[70:73], v[126:129]
	v_mfma_f32_16x16x32_bf16 v[2:5], v[154:157], v[70:73], v[2:5]
	v_mfma_f32_16x16x32_bf16 v[234:237], v[110:113], v[70:73], v[98:101]
	s_waitcnt lgkmcnt(5)
	v_mfma_f32_16x16x32_bf16 v[126:129], v[166:169], v[82:85], v[34:37]
	s_nop 2
	ds_read_b128 v[34:37], v244 offset:36864
	v_mfma_f32_16x16x32_bf16 v[122:125], v[214:217], v[82:85], v[38:41]
	s_waitcnt lgkmcnt(4)
	v_mfma_f32_16x16x32_bf16 v[118:121], v[230:233], v[82:85], v[42:45]
	s_waitcnt lgkmcnt(1)
	v_mfma_f32_16x16x32_bf16 v[114:117], v[142:145], v[82:85], v[30:33]
	s_nop 2
	ds_read_b128 v[30:33], v244 offset:38912
	v_mfma_f32_16x16x32_bf16 v[110:113], v[166:169], v[86:89], v[46:49]
	v_mfma_f32_16x16x32_bf16 v[106:109], v[214:217], v[86:89], v[50:53]
	v_mfma_f32_16x16x32_bf16 v[102:105], v[230:233], v[86:89], v[58:61]
	v_mfma_f32_16x16x32_bf16 v[98:101], v[142:145], v[86:89], v[26:29]
	s_nop 2
	ds_read_b128 v[26:29], v244 offset:40960
	s_waitcnt lgkmcnt(2)
	v_mfma_f32_16x16x32_bf16 v[94:97], v[166:169], v[34:37], v[62:65]
	v_mfma_f32_16x16x32_bf16 v[90:93], v[214:217], v[34:37], v[66:69]
	v_mfma_f32_16x16x32_bf16 v[86:89], v[230:233], v[34:37], v[74:77]
	v_mfma_f32_16x16x32_bf16 v[82:85], v[142:145], v[34:37], v[22:25]
	s_nop 2
	ds_read_b128 v[22:25], v244 offset:43008
	s_waitcnt lgkmcnt(2)
	v_mfma_f32_16x16x32_bf16 v[78:81], v[166:169], v[30:33], v[78:81]
	v_mfma_f32_16x16x32_bf16 v[74:77], v[214:217], v[30:33], v[150:153]
	v_mfma_f32_16x16x32_bf16 v[70:73], v[230:233], v[30:33], v[158:161]
	v_mfma_f32_16x16x32_bf16 v[66:69], v[142:145], v[30:33], v[18:21]
	s_nop 2
	ds_read_b128 v[18:21], v244 offset:45056
	s_waitcnt lgkmcnt(2)
	v_mfma_f32_16x16x32_bf16 v[62:65], v[166:169], v[26:29], v[54:57]
	v_mfma_f32_16x16x32_bf16 v[58:61], v[214:217], v[26:29], v[138:141]
	v_mfma_f32_16x16x32_bf16 v[54:57], v[230:233], v[26:29], v[162:165]
	v_mfma_f32_16x16x32_bf16 v[50:53], v[142:145], v[26:29], v[14:17]
	s_waitcnt lgkmcnt(1)
	v_mfma_f32_16x16x32_bf16 v[46:49], v[166:169], v[22:25], v[146:149]
	ds_read_b128 v[138:141], v244 offset:47104
	v_mfma_f32_16x16x32_bf16 v[42:45], v[214:217], v[22:25], v[206:209]
	v_mfma_f32_16x16x32_bf16 v[38:41], v[230:233], v[22:25], v[210:213]
	v_mfma_f32_16x16x32_bf16 v[34:37], v[142:145], v[22:25], v[10:13]
	s_waitcnt lgkmcnt(1)
	v_mfma_f32_16x16x32_bf16 v[30:33], v[166:169], v[18:21], v[218:221]
	v_mfma_f32_16x16x32_bf16 v[26:29], v[214:217], v[18:21], v[222:225]
	v_mfma_f32_16x16x32_bf16 v[22:25], v[230:233], v[18:21], v[226:229]
	v_mfma_f32_16x16x32_bf16 v[18:21], v[142:145], v[18:21], v[6:9]
	s_waitcnt lgkmcnt(0)
	v_mfma_f32_16x16x32_bf16 v[14:17], v[166:169], v[138:141], v[234:237]
	v_mfma_f32_16x16x32_bf16 v[10:13], v[214:217], v[138:141], v[134:137]
	v_mfma_f32_16x16x32_bf16 v[6:9], v[230:233], v[138:141], v[130:133]
	v_mfma_f32_16x16x32_bf16 v[2:5], v[142:145], v[138:141], v[2:5]
	s_waitcnt lgkmcnt(0)
	s_barrier
	s_nop 0
	v_mov_b32_e32 v131, 0
	s_andn2_b64 vcc, exec, s[12:13]
	v_mov_b32_e32 v133, 0
	v_mov_b32_e32 v134, 0
	s_cbranch_vccnz .LBB0_1536
	global_load_dword v131, v[184:185], off
	global_load_dword v133, v[186:187], off
	global_load_dword v134, v[188:189], off
	s_branch .LBB0_1536
